# baseline (speedup 1.0000x reference)
_Z11attn_kernelILi0EEvPKDF16_S1_S1_PKfS3_PfPDF16_:
	v_readfirstlane_b32 s3, v0
	s_lshr_b32 s14, s3, 6
	s_lshl_b32 s3, s2, 7
	s_lshr_b32 s12, s2, 4
	s_and_b32 s3, s3, 0x780
	s_lshl_b32 s4, s14, 5
	s_mov_b32 s13, 0
	s_load_dwordx4 s[8:11], s[0:1], 0x0
	s_load_dwordx2 s[18:19], s[0:1], 0x10
	s_add_i32 s3, s4, s3
	s_lshl_b64 s[4:5], s[12:13], 11
	s_add_u32 s16, s4, s3
	s_addc_u32 s17, s5, 0
	s_lshl_b64 s[4:5], s[16:17], 7
	v_and_b32_e32 v164, 31, v0
	s_waitcnt lgkmcnt(0)
	s_add_u32 s4, s8, s4
	v_bfe_u32 v72, v0, 5, 1
	s_addc_u32 s5, s9, s5
	s_lshl_b64 s[22:23], s[12:13], 18
	v_lshlrev_b32_e32 v128, 7, v164
	v_mov_b32_e32 v129, 0
	s_add_u32 s8, s10, s22
	v_lshl_add_u64 v[2:3], s[4:5], 0, v[128:129]
	v_lshlrev_b32_e32 v128, 4, v72
	s_addc_u32 s9, s11, s23
	v_lshl_add_u64 v[10:11], v[2:3], 0, v[128:129]
	v_or_b32_e32 v12, 0x100, v0
	v_lshlrev_b32_e32 v128, 4, v0
	v_lshlrev_b32_e32 v44, 4, v12
	global_load_dwordx4 v[2:5], v128, s[8:9]
	global_load_dwordx4 v[6:9], v44, s[8:9]
	v_lshlrev_b32_e32 v79, 3, v0
	s_movk_i32 s4, 0x48
	v_lshrrev_b32_e32 v73, 3, v0
	v_and_b32_e32 v74, 56, v79
	v_lshrrev_b32_e32 v75, 3, v12
	v_mad_u32_u24 v165, v75, s4, v74
	v_mad_u32_u24 v166, v73, s4, v74
	global_load_dwordx4 v[108:111], v[10:11], off
	global_load_dwordx4 v[104:107], v[10:11], off offset:32
	global_load_dwordx4 v[100:103], v[10:11], off offset:64
	global_load_dwordx4 v[96:99], v[10:11], off offset:96
	v_mov_b32_e32 v86, v44
	s_add_u32 s24, s8, 0x2000
	s_addc_u32 s25, s9, 0
	global_load_dwordx4 v[120:123], v128, s[24:25]
	global_load_dwordx4 v[124:127], v44, s[24:25]
	s_add_u32 s24, s24, 0x2000
	s_addc_u32 s25, s25, 0
	global_load_dwordx4 v[146:149], v128, s[24:25]
	global_load_dwordx4 v[150:153], v44, s[24:25]
	s_add_u32 s24, s24, 0x2000
	s_addc_u32 s25, s25, 0
	global_load_dwordx4 v[154:157], v128, s[24:25]
	global_load_dwordx4 v[158:161], v44, s[24:25]
	s_add_u32 s24, s24, 0x2000
	s_addc_u32 s25, s25, 0
	s_add_u32 s4, s8, 0x2000
	v_lshlrev_b32_e32 v13, 1, v166
	s_addc_u32 s5, s9, 0
	v_lshlrev_b32_e32 v14, 1, v165
	v_lshlrev_b32_e32 v1, 3, v72
	v_mul_u32_u24_e32 v76, 0x48, v164
	v_lshlrev_b32_e32 v80, 3, v12
	v_mov_b32_e32 v45, v129
	s_mov_b32 s15, 1
	v_add_u32_e32 v77, 0x6000, v13
	v_add_u32_e32 v78, 0x6000, v14
	s_waitcnt vmcnt(11)
	ds_write_b128 v13, v[2:5] offset:24576
	s_waitcnt vmcnt(10)
	ds_write_b128 v14, v[6:9] offset:24576
	s_waitcnt lgkmcnt(0)
	s_barrier
	s_load_dwordx4 s[4:7], s[0:1], 0x28
	v_lshlrev_b32_e32 v88, 1, v166
	v_lshlrev_b32_e32 v89, 1, v165
	ds_write_b128 v88, v[2:5]
	ds_write_b128 v89, v[6:9]
	v_add_lshl_u32 v87, v1, v76, 1
	v_add_u32_e32 v167, 0x9000, v87
	v_add_u32_e32 v77, 0x9000, v88
	v_add_u32_e32 v78, 0x9000, v89
	v_lshl_add_u64 v[68:69], s[8:9], 0, v[44:45]
	v_lshl_add_u64 v[66:67], s[8:9], 0, v[128:129]
	s_lshl_b64 s[20:21], s[12:13], 17
	v_mov_b32_e32 v81, 0
	v_mov_b32_e32 v82, 0
	v_mov_b32_e32 v130, 0
	v_mov_b32_e32 v131, 0
	v_mov_b32_e32 v132, 0
	v_mov_b32_e32 v133, 0
	v_mov_b32_e32 v134, 0
	v_mov_b32_e32 v135, 0
	v_mov_b32_e32 v136, 0
	v_mov_b32_e32 v137, 0
	v_mov_b32_e32 v138, 0
	v_mov_b32_e32 v139, 0
	v_mov_b32_e32 v140, 0
	v_mov_b32_e32 v141, 0
	v_mov_b32_e32 v142, 0
	v_mov_b32_e32 v143, 0
	v_mov_b32_e32 v144, 0
	v_mov_b32_e32 v145, 0
	s_mov_b32 s11, 0xff800000
	s_mov_b32 s15, 0
	s_waitcnt vmcnt(0) lgkmcnt(0)
	ds_write_b128 v88, v[120:123] offset:9216
	ds_write_b128 v89, v[124:127] offset:9216
	ds_write_b128 v88, v[146:149] offset:18432
	ds_write_b128 v89, v[150:153] offset:18432
	ds_write_b128 v88, v[154:157] offset:27648
	ds_write_b128 v89, v[158:161] offset:27648
	v_mov_b32_e32 v34, 0xff800000
	v_mov_b32_e32 v35, v34
	v_mov_b32_e32 v36, v34
	v_mov_b32_e32 v37, v34
	v_mov_b32_e32 v38, v34
	v_mov_b32_e32 v39, v34
	v_mov_b32_e32 v40, v34
	v_mov_b32_e32 v41, v34
	v_mov_b32_e32 v42, v34
	v_mov_b32_e32 v43, v34
	v_mov_b32_e32 v44, v34
	v_mov_b32_e32 v45, v34
	v_mov_b32_e32 v46, v34
	v_mov_b32_e32 v47, v34
	v_mov_b32_e32 v48, v34
	v_mov_b32_e32 v49, v34
	v_mov_b32_e32 v50, v34
	v_mov_b32_e32 v51, v34
	v_mov_b32_e32 v52, v34
	v_mov_b32_e32 v53, v34
	v_mov_b32_e32 v54, v34
	v_mov_b32_e32 v55, v34
	v_mov_b32_e32 v56, v34
	v_mov_b32_e32 v57, v34
	v_mov_b32_e32 v58, v34
	v_mov_b32_e32 v59, v34
	v_mov_b32_e32 v60, v34
	v_mov_b32_e32 v61, v34
	v_mov_b32_e32 v62, v34
	v_mov_b32_e32 v63, v34
	v_mov_b32_e32 v64, v34
	v_mov_b32_e32 v65, v34
	global_load_dwordx4 v[112:115], v128, s[24:25]
	global_load_dwordx4 v[116:119], v86, s[24:25]
	s_add_u32 s24, s24, 0x2000
	s_addc_u32 s25, s25, 0
	global_load_dwordx4 v[120:123], v128, s[24:25]
	global_load_dwordx4 v[124:127], v86, s[24:25]
	s_add_u32 s24, s24, 0x2000
	s_addc_u32 s25, s25, 0
	global_load_dwordx4 v[146:149], v128, s[24:25]
	global_load_dwordx4 v[150:153], v86, s[24:25]
	s_add_u32 s24, s24, 0x2000
	s_addc_u32 s25, s25, 0
	global_load_dwordx4 v[154:157], v128, s[24:25]
	global_load_dwordx4 v[158:161], v86, s[24:25]
	s_add_u32 s24, s24, 0x2000
	s_addc_u32 s25, s25, 0
	s_waitcnt lgkmcnt(0)
	s_barrier
.Lp1_loop:
	s_waitcnt vmcnt(0)
	ds_write_b128 v77, v[112:115]
	ds_write_b128 v78, v[116:119]
	ds_write_b128 v77, v[120:123] offset:9216
	ds_write_b128 v78, v[124:127] offset:9216
	ds_write_b128 v77, v[146:149] offset:18432
	ds_write_b128 v78, v[150:153] offset:18432
	ds_write_b128 v77, v[154:157] offset:27648
	ds_write_b128 v78, v[158:161] offset:27648
	global_load_dwordx4 v[112:115], v128, s[24:25]
	global_load_dwordx4 v[116:119], v86, s[24:25]
	s_add_u32 s24, s24, 0x2000
	s_addc_u32 s25, s25, 0
	global_load_dwordx4 v[120:123], v128, s[24:25]
	global_load_dwordx4 v[124:127], v86, s[24:25]
	s_add_u32 s24, s24, 0x2000
	s_addc_u32 s25, s25, 0
	global_load_dwordx4 v[146:149], v128, s[24:25]
	global_load_dwordx4 v[150:153], v86, s[24:25]
	s_add_u32 s24, s24, 0x2000
	s_addc_u32 s25, s25, 0
	global_load_dwordx4 v[154:157], v128, s[24:25]
	global_load_dwordx4 v[158:161], v86, s[24:25]
	s_add_u32 s24, s24, 0x2000
	s_addc_u32 s25, s25, 0
	ds_read_b128 v[168:171], v87
	ds_read_b128 v[172:175], v87 offset:4608
	ds_read_b128 v[176:179], v87 offset:32
	ds_read_b128 v[180:183], v87 offset:4640
	ds_read_b128 v[184:187], v87 offset:64
	ds_read_b128 v[188:191], v87 offset:4672
	ds_read_b128 v[192:195], v87 offset:96
	ds_read_b128 v[196:199], v87 offset:4704
	v_mov_b32_e32 v200, 0
	v_mov_b32_e32 v201, 0
	v_mov_b32_e32 v202, 0
	v_mov_b32_e32 v83, 0
	v_exp_f32_e32 v34, v34
	v_exp_f32_e32 v35, v35
	v_add_f32_e32 v200, v200, v34
	v_exp_f32_e32 v36, v36
	v_add_f32_e32 v201, v201, v35
	v_exp_f32_e32 v37, v37
	s_waitcnt lgkmcnt(7)
	v_mfma_f32_32x32x16_f16 v[2:17], v[168:171], v[108:111], v[130:145]
	v_add_f32_e32 v202, v202, v36
	v_exp_f32_e32 v38, v38
	v_add_f32_e32 v83, v83, v37
	v_exp_f32_e32 v39, v39
	v_add_f32_e32 v200, v200, v38
	v_exp_f32_e32 v40, v40
	s_waitcnt lgkmcnt(6)
	v_mfma_f32_32x32x16_f16 v[18:33], v[172:175], v[108:111], v[130:145]
	v_add_f32_e32 v201, v201, v39
	v_exp_f32_e32 v41, v41
	v_add_f32_e32 v202, v202, v40
	v_exp_f32_e32 v42, v42
	v_add_f32_e32 v83, v83, v41
	v_exp_f32_e32 v43, v43
	s_waitcnt lgkmcnt(5)
	v_mfma_f32_32x32x16_f16 v[2:17], v[176:179], v[104:107], v[2:17]
	v_add_f32_e32 v200, v200, v42
	v_exp_f32_e32 v44, v44
	v_add_f32_e32 v201, v201, v43
	v_exp_f32_e32 v45, v45
	v_add_f32_e32 v202, v202, v44
	v_exp_f32_e32 v46, v46
	s_waitcnt lgkmcnt(4)
	v_mfma_f32_32x32x16_f16 v[18:33], v[180:183], v[104:107], v[18:33]
	v_add_f32_e32 v83, v83, v45
	v_exp_f32_e32 v47, v47
	v_add_f32_e32 v200, v200, v46
	v_exp_f32_e32 v48, v48
	v_add_f32_e32 v201, v201, v47
	v_exp_f32_e32 v49, v49
	s_waitcnt lgkmcnt(3)
	v_mfma_f32_32x32x16_f16 v[2:17], v[184:187], v[100:103], v[2:17]
	v_add_f32_e32 v202, v202, v48
	v_exp_f32_e32 v50, v50
	v_add_f32_e32 v83, v83, v49
	v_exp_f32_e32 v51, v51
	v_add_f32_e32 v200, v200, v50
	v_exp_f32_e32 v52, v52
	s_waitcnt lgkmcnt(2)
	v_mfma_f32_32x32x16_f16 v[18:33], v[188:191], v[100:103], v[18:33]
	v_add_f32_e32 v201, v201, v51
	v_exp_f32_e32 v53, v53
	v_add_f32_e32 v202, v202, v52
	v_exp_f32_e32 v54, v54
	v_add_f32_e32 v83, v83, v53
	v_exp_f32_e32 v55, v55
	s_waitcnt lgkmcnt(1)
	v_mfma_f32_32x32x16_f16 v[2:17], v[192:195], v[96:99], v[2:17]
	v_add_f32_e32 v200, v200, v54
	v_exp_f32_e32 v56, v56
	v_add_f32_e32 v201, v201, v55
	v_exp_f32_e32 v57, v57
	v_add_f32_e32 v202, v202, v56
	v_exp_f32_e32 v58, v58
	s_waitcnt lgkmcnt(0)
	v_mfma_f32_32x32x16_f16 v[18:33], v[196:199], v[96:99], v[18:33]
	ds_read_b128 v[204:207], v87 offset:9216
	ds_read_b128 v[208:211], v87 offset:13824
	ds_read_b128 v[212:215], v87 offset:9248
	ds_read_b128 v[216:219], v87 offset:13856
	ds_read_b128 v[220:223], v87 offset:9280
	ds_read_b128 v[224:227], v87 offset:13888
	ds_read_b128 v[228:231], v87 offset:9312
	ds_read_b128 v[232:235], v87 offset:13920
	v_add_f32_e32 v83, v83, v57
	v_exp_f32_e32 v59, v59
	v_add_f32_e32 v200, v200, v58
	v_exp_f32_e32 v60, v60
	v_add_f32_e32 v201, v201, v59
	v_exp_f32_e32 v61, v61
	v_add_f32_e32 v202, v202, v60
	v_exp_f32_e32 v62, v62
	v_add_f32_e32 v83, v83, v61
	v_exp_f32_e32 v63, v63
	v_add_f32_e32 v200, v200, v62
	v_exp_f32_e32 v64, v64
	v_add_f32_e32 v201, v201, v63
	v_exp_f32_e32 v65, v65
	v_add_f32_e32 v202, v202, v64
	v_add_f32_e32 v83, v83, v65
	v_add_f32_e32 v200, v200, v201
	v_add_f32_e32 v202, v202, v83
	v_add_f32_e32 v200, v200, v202
	v_add_f32_e32 v82, v82, v200
	v_max3_f32 v84, v2, v3, v4
	v_max3_f32 v85, v18, v19, v20
	v_max3_f32 v84, v84, v5, v6
	v_max3_f32 v85, v85, v21, v22
	v_max3_f32 v84, v84, v7, v8
	v_max3_f32 v85, v85, v23, v24
	v_max3_f32 v84, v84, v9, v10
	v_max3_f32 v85, v85, v25, v26
	v_max3_f32 v84, v84, v11, v12
	v_max3_f32 v85, v85, v27, v28
	v_max3_f32 v84, v84, v13, v14
	v_max3_f32 v85, v85, v29, v30
	v_max3_f32 v84, v84, v15, v16
	v_max3_f32 v85, v85, v31, v32
	v_max3_f32 v84, v84, v17, v33
	s_nop 0
	v_max_f32_e32 v84, v84, v85
	s_nop 0
	v_cmp_lt_f32_e32 vcc, s11, v84
	s_cbranch_vccnz .Lp1_rare_d0t0
.Lp1_back_d0t0:
	v_mov_b32_e32 v200, 0
	v_mov_b32_e32 v201, 0
	v_mov_b32_e32 v202, 0
	v_mov_b32_e32 v83, 0
	v_exp_f32_e32 v2, v2
	v_exp_f32_e32 v3, v3
	v_add_f32_e32 v200, v200, v2
	v_exp_f32_e32 v4, v4
	v_add_f32_e32 v201, v201, v3
	v_exp_f32_e32 v5, v5
	s_waitcnt lgkmcnt(7)
	v_mfma_f32_32x32x16_f16 v[34:49], v[204:207], v[108:111], v[130:145]
	v_add_f32_e32 v202, v202, v4
	v_exp_f32_e32 v6, v6
	v_add_f32_e32 v83, v83, v5
	v_exp_f32_e32 v7, v7
	v_add_f32_e32 v200, v200, v6
	v_exp_f32_e32 v8, v8
	s_waitcnt lgkmcnt(6)
	v_mfma_f32_32x32x16_f16 v[50:65], v[208:211], v[108:111], v[130:145]
	v_add_f32_e32 v201, v201, v7
	v_exp_f32_e32 v9, v9
	v_add_f32_e32 v202, v202, v8
	v_exp_f32_e32 v10, v10
	v_add_f32_e32 v83, v83, v9
	v_exp_f32_e32 v11, v11
	s_waitcnt lgkmcnt(5)
	v_mfma_f32_32x32x16_f16 v[34:49], v[212:215], v[104:107], v[34:49]
	v_add_f32_e32 v200, v200, v10
	v_exp_f32_e32 v12, v12
	v_add_f32_e32 v201, v201, v11
	v_exp_f32_e32 v13, v13
	v_add_f32_e32 v202, v202, v12
	v_exp_f32_e32 v14, v14
	s_waitcnt lgkmcnt(4)
	v_mfma_f32_32x32x16_f16 v[50:65], v[216:219], v[104:107], v[50:65]
	v_add_f32_e32 v83, v83, v13
	v_exp_f32_e32 v15, v15
	v_add_f32_e32 v200, v200, v14
	v_exp_f32_e32 v16, v16
	v_add_f32_e32 v201, v201, v15
	v_exp_f32_e32 v17, v17
	s_waitcnt lgkmcnt(3)
	v_mfma_f32_32x32x16_f16 v[34:49], v[220:223], v[100:103], v[34:49]
	v_add_f32_e32 v202, v202, v16
	v_exp_f32_e32 v18, v18
	v_add_f32_e32 v83, v83, v17
	v_exp_f32_e32 v19, v19
	v_add_f32_e32 v200, v200, v18
	v_exp_f32_e32 v20, v20
	s_waitcnt lgkmcnt(2)
	v_mfma_f32_32x32x16_f16 v[50:65], v[224:227], v[100:103], v[50:65]
	v_add_f32_e32 v201, v201, v19
	v_exp_f32_e32 v21, v21
	v_add_f32_e32 v202, v202, v20
	v_exp_f32_e32 v22, v22
	v_add_f32_e32 v83, v83, v21
	v_exp_f32_e32 v23, v23
	s_waitcnt lgkmcnt(1)
	v_mfma_f32_32x32x16_f16 v[34:49], v[228:231], v[96:99], v[34:49]
	v_add_f32_e32 v200, v200, v22
	v_exp_f32_e32 v24, v24
	v_add_f32_e32 v201, v201, v23
	v_exp_f32_e32 v25, v25
	v_add_f32_e32 v202, v202, v24
	v_exp_f32_e32 v26, v26
	s_waitcnt lgkmcnt(0)
	v_mfma_f32_32x32x16_f16 v[50:65], v[232:235], v[96:99], v[50:65]
	ds_read_b128 v[168:171], v87 offset:18432
	ds_read_b128 v[172:175], v87 offset:23040
	ds_read_b128 v[176:179], v87 offset:18464
	ds_read_b128 v[180:183], v87 offset:23072
	ds_read_b128 v[184:187], v87 offset:18496
	ds_read_b128 v[188:191], v87 offset:23104
	ds_read_b128 v[192:195], v87 offset:18528
	ds_read_b128 v[196:199], v87 offset:23136
	v_add_f32_e32 v83, v83, v25
	v_exp_f32_e32 v27, v27
	v_add_f32_e32 v200, v200, v26
	v_exp_f32_e32 v28, v28
	v_add_f32_e32 v201, v201, v27
	v_exp_f32_e32 v29, v29
	v_add_f32_e32 v202, v202, v28
	v_exp_f32_e32 v30, v30
	v_add_f32_e32 v83, v83, v29
	v_exp_f32_e32 v31, v31
	v_add_f32_e32 v200, v200, v30
	v_exp_f32_e32 v32, v32
	v_add_f32_e32 v201, v201, v31
	v_exp_f32_e32 v33, v33
	v_add_f32_e32 v202, v202, v32
	v_add_f32_e32 v83, v83, v33
	v_add_f32_e32 v200, v200, v201
	v_add_f32_e32 v202, v202, v83
	v_add_f32_e32 v200, v200, v202
	v_add_f32_e32 v82, v82, v200
	v_max3_f32 v84, v34, v35, v36
	v_max3_f32 v85, v50, v51, v52
	v_max3_f32 v84, v84, v37, v38
	v_max3_f32 v85, v85, v53, v54
	v_max3_f32 v84, v84, v39, v40
	v_max3_f32 v85, v85, v55, v56
	v_max3_f32 v84, v84, v41, v42
	v_max3_f32 v85, v85, v57, v58
	v_max3_f32 v84, v84, v43, v44
	v_max3_f32 v85, v85, v59, v60
	v_max3_f32 v84, v84, v45, v46
	v_max3_f32 v85, v85, v61, v62
	v_max3_f32 v84, v84, v47, v48
	v_max3_f32 v85, v85, v63, v64
	v_max3_f32 v84, v84, v49, v65
	s_nop 0
	v_max_f32_e32 v84, v84, v85
	s_nop 0
	v_cmp_lt_f32_e32 vcc, s11, v84
	s_cbranch_vccnz .Lp1_rare_d0t1
.Lp1_back_d0t1:
	v_mov_b32_e32 v200, 0
	v_mov_b32_e32 v201, 0
	v_mov_b32_e32 v202, 0
	v_mov_b32_e32 v83, 0
	v_exp_f32_e32 v34, v34
	v_exp_f32_e32 v35, v35
	v_add_f32_e32 v200, v200, v34
	v_exp_f32_e32 v36, v36
	v_add_f32_e32 v201, v201, v35
	v_exp_f32_e32 v37, v37
	s_waitcnt lgkmcnt(7)
	v_mfma_f32_32x32x16_f16 v[2:17], v[168:171], v[108:111], v[130:145]
	v_add_f32_e32 v202, v202, v36
	v_exp_f32_e32 v38, v38
	v_add_f32_e32 v83, v83, v37
	v_exp_f32_e32 v39, v39
	v_add_f32_e32 v200, v200, v38
	v_exp_f32_e32 v40, v40
	s_waitcnt lgkmcnt(6)
	v_mfma_f32_32x32x16_f16 v[18:33], v[172:175], v[108:111], v[130:145]
	v_add_f32_e32 v201, v201, v39
	v_exp_f32_e32 v41, v41
	v_add_f32_e32 v202, v202, v40
	v_exp_f32_e32 v42, v42
	v_add_f32_e32 v83, v83, v41
	v_exp_f32_e32 v43, v43
	s_waitcnt lgkmcnt(5)
	v_mfma_f32_32x32x16_f16 v[2:17], v[176:179], v[104:107], v[2:17]
	v_add_f32_e32 v200, v200, v42
	v_exp_f32_e32 v44, v44
	v_add_f32_e32 v201, v201, v43
	v_exp_f32_e32 v45, v45
	v_add_f32_e32 v202, v202, v44
	v_exp_f32_e32 v46, v46
	s_waitcnt lgkmcnt(4)
	v_mfma_f32_32x32x16_f16 v[18:33], v[180:183], v[104:107], v[18:33]
	v_add_f32_e32 v83, v83, v45
	v_exp_f32_e32 v47, v47
	v_add_f32_e32 v200, v200, v46
	v_exp_f32_e32 v48, v48
	v_add_f32_e32 v201, v201, v47
	v_exp_f32_e32 v49, v49
	s_waitcnt lgkmcnt(3)
	v_mfma_f32_32x32x16_f16 v[2:17], v[184:187], v[100:103], v[2:17]
	v_add_f32_e32 v202, v202, v48
	v_exp_f32_e32 v50, v50
	v_add_f32_e32 v83, v83, v49
	v_exp_f32_e32 v51, v51
	v_add_f32_e32 v200, v200, v50
	v_exp_f32_e32 v52, v52
	s_waitcnt lgkmcnt(2)
	v_mfma_f32_32x32x16_f16 v[18:33], v[188:191], v[100:103], v[18:33]
	v_add_f32_e32 v201, v201, v51
	v_exp_f32_e32 v53, v53
	v_add_f32_e32 v202, v202, v52
	v_exp_f32_e32 v54, v54
	v_add_f32_e32 v83, v83, v53
	v_exp_f32_e32 v55, v55
	s_waitcnt lgkmcnt(1)
	v_mfma_f32_32x32x16_f16 v[2:17], v[192:195], v[96:99], v[2:17]
	v_add_f32_e32 v200, v200, v54
	v_exp_f32_e32 v56, v56
	v_add_f32_e32 v201, v201, v55
	v_exp_f32_e32 v57, v57
	v_add_f32_e32 v202, v202, v56
	v_exp_f32_e32 v58, v58
	s_waitcnt lgkmcnt(0)
	v_mfma_f32_32x32x16_f16 v[18:33], v[196:199], v[96:99], v[18:33]
	ds_read_b128 v[204:207], v87 offset:27648
	ds_read_b128 v[208:211], v87 offset:32256
	ds_read_b128 v[212:215], v87 offset:27680
	ds_read_b128 v[216:219], v87 offset:32288
	ds_read_b128 v[220:223], v87 offset:27712
	ds_read_b128 v[224:227], v87 offset:32320
	ds_read_b128 v[228:231], v87 offset:27744
	ds_read_b128 v[232:235], v87 offset:32352
	v_add_f32_e32 v83, v83, v57
	v_exp_f32_e32 v59, v59
	v_add_f32_e32 v200, v200, v58
	v_exp_f32_e32 v60, v60
	v_add_f32_e32 v201, v201, v59
	v_exp_f32_e32 v61, v61
	v_add_f32_e32 v202, v202, v60
	v_exp_f32_e32 v62, v62
	v_add_f32_e32 v83, v83, v61
	v_exp_f32_e32 v63, v63
	v_add_f32_e32 v200, v200, v62
	v_exp_f32_e32 v64, v64
	v_add_f32_e32 v201, v201, v63
	v_exp_f32_e32 v65, v65
	v_add_f32_e32 v202, v202, v64
	v_add_f32_e32 v83, v83, v65
	v_add_f32_e32 v200, v200, v201
	v_add_f32_e32 v202, v202, v83
	v_add_f32_e32 v200, v200, v202
	v_add_f32_e32 v82, v82, v200
	v_max3_f32 v84, v2, v3, v4
	v_max3_f32 v85, v18, v19, v20
	v_max3_f32 v84, v84, v5, v6
	v_max3_f32 v85, v85, v21, v22
	v_max3_f32 v84, v84, v7, v8
	v_max3_f32 v85, v85, v23, v24
	v_max3_f32 v84, v84, v9, v10
	v_max3_f32 v85, v85, v25, v26
	v_max3_f32 v84, v84, v11, v12
	v_max3_f32 v85, v85, v27, v28
	v_max3_f32 v84, v84, v13, v14
	v_max3_f32 v85, v85, v29, v30
	v_max3_f32 v84, v84, v15, v16
	v_max3_f32 v85, v85, v31, v32
	v_max3_f32 v84, v84, v17, v33
	s_nop 0
	v_max_f32_e32 v84, v84, v85
	s_nop 0
	v_cmp_lt_f32_e32 vcc, s11, v84
	s_cbranch_vccnz .Lp1_rare_d0t2

.Lp1_back_d0t3:
	s_waitcnt lgkmcnt(0)
	s_barrier
	s_waitcnt vmcnt(0)
	ds_write_b128 v88, v[112:115]
	ds_write_b128 v89, v[116:119]
	ds_write_b128 v88, v[120:123] offset:9216
	ds_write_b128 v89, v[124:127] offset:9216
	ds_write_b128 v88, v[146:149] offset:18432
	ds_write_b128 v89, v[150:153] offset:18432
	ds_write_b128 v88, v[154:157] offset:27648
	ds_write_b128 v89, v[158:161] offset:27648
	global_load_dwordx4 v[112:115], v128, s[24:25]
	global_load_dwordx4 v[116:119], v86, s[24:25]
	s_add_u32 s24, s24, 0x2000
	s_addc_u32 s25, s25, 0
	global_load_dwordx4 v[120:123], v128, s[24:25]
	global_load_dwordx4 v[124:127], v86, s[24:25]
	s_add_u32 s24, s24, 0x2000
	s_addc_u32 s25, s25, 0
	global_load_dwordx4 v[146:149], v128, s[24:25]
	global_load_dwordx4 v[150:153], v86, s[24:25]
	s_add_u32 s24, s24, 0x2000
	s_addc_u32 s25, s25, 0
	global_load_dwordx4 v[154:157], v128, s[24:25]
	global_load_dwordx4 v[158:161], v86, s[24:25]
	s_add_u32 s24, s24, 0x2000
	s_addc_u32 s25, s25, 0
	ds_read_b128 v[168:171], v167
	ds_read_b128 v[172:175], v167 offset:4608
	ds_read_b128 v[176:179], v167 offset:32
	ds_read_b128 v[180:183], v167 offset:4640
	ds_read_b128 v[184:187], v167 offset:64
	ds_read_b128 v[188:191], v167 offset:4672
	ds_read_b128 v[192:195], v167 offset:96
	ds_read_b128 v[196:199], v167 offset:4704
	v_mov_b32_e32 v200, 0
	v_mov_b32_e32 v201, 0
	v_mov_b32_e32 v202, 0
	v_mov_b32_e32 v83, 0
	v_exp_f32_e32 v34, v34
	v_exp_f32_e32 v35, v35
	v_add_f32_e32 v200, v200, v34
	v_exp_f32_e32 v36, v36
	v_add_f32_e32 v201, v201, v35
	v_exp_f32_e32 v37, v37
	s_waitcnt lgkmcnt(7)
	v_mfma_f32_32x32x16_f16 v[2:17], v[168:171], v[108:111], v[130:145]
	v_add_f32_e32 v202, v202, v36
	v_exp_f32_e32 v38, v38
	v_add_f32_e32 v83, v83, v37
	v_exp_f32_e32 v39, v39
	v_add_f32_e32 v200, v200, v38
	v_exp_f32_e32 v40, v40
	s_waitcnt lgkmcnt(6)
	v_mfma_f32_32x32x16_f16 v[18:33], v[172:175], v[108:111], v[130:145]
	v_add_f32_e32 v201, v201, v39
	v_exp_f32_e32 v41, v41
	v_add_f32_e32 v202, v202, v40
	v_exp_f32_e32 v42, v42
	v_add_f32_e32 v83, v83, v41
	v_exp_f32_e32 v43, v43
	s_waitcnt lgkmcnt(5)
	v_mfma_f32_32x32x16_f16 v[2:17], v[176:179], v[104:107], v[2:17]
	v_add_f32_e32 v200, v200, v42
	v_exp_f32_e32 v44, v44
	v_add_f32_e32 v201, v201, v43
	v_exp_f32_e32 v45, v45
	v_add_f32_e32 v202, v202, v44
	v_exp_f32_e32 v46, v46
	s_waitcnt lgkmcnt(4)
	v_mfma_f32_32x32x16_f16 v[18:33], v[180:183], v[104:107], v[18:33]
	v_add_f32_e32 v83, v83, v45
	v_exp_f32_e32 v47, v47
	v_add_f32_e32 v200, v200, v46
	v_exp_f32_e32 v48, v48
	v_add_f32_e32 v201, v201, v47
	v_exp_f32_e32 v49, v49
	s_waitcnt lgkmcnt(3)
	v_mfma_f32_32x32x16_f16 v[2:17], v[184:187], v[100:103], v[2:17]
	v_add_f32_e32 v202, v202, v48
	v_exp_f32_e32 v50, v50
	v_add_f32_e32 v83, v83, v49
	v_exp_f32_e32 v51, v51
	v_add_f32_e32 v200, v200, v50
	v_exp_f32_e32 v52, v52
	s_waitcnt lgkmcnt(2)
	v_mfma_f32_32x32x16_f16 v[18:33], v[188:191], v[100:103], v[18:33]
	v_add_f32_e32 v201, v201, v51
	v_exp_f32_e32 v53, v53
	v_add_f32_e32 v202, v202, v52
	v_exp_f32_e32 v54, v54
	v_add_f32_e32 v83, v83, v53
	v_exp_f32_e32 v55, v55
	s_waitcnt lgkmcnt(1)
	v_mfma_f32_32x32x16_f16 v[2:17], v[192:195], v[96:99], v[2:17]
	v_add_f32_e32 v200, v200, v54
	v_exp_f32_e32 v56, v56
	v_add_f32_e32 v201, v201, v55
	v_exp_f32_e32 v57, v57
	v_add_f32_e32 v202, v202, v56
	v_exp_f32_e32 v58, v58
	s_waitcnt lgkmcnt(0)
	v_mfma_f32_32x32x16_f16 v[18:33], v[196:199], v[96:99], v[18:33]
	ds_read_b128 v[204:207], v167 offset:9216
	ds_read_b128 v[208:211], v167 offset:13824
	ds_read_b128 v[212:215], v167 offset:9248
	ds_read_b128 v[216:219], v167 offset:13856
	ds_read_b128 v[220:223], v167 offset:9280
	ds_read_b128 v[224:227], v167 offset:13888
	ds_read_b128 v[228:231], v167 offset:9312
	ds_read_b128 v[232:235], v167 offset:13920
	v_add_f32_e32 v83, v83, v57
	v_exp_f32_e32 v59, v59
	v_add_f32_e32 v200, v200, v58
	v_exp_f32_e32 v60, v60
	v_add_f32_e32 v201, v201, v59
	v_exp_f32_e32 v61, v61
	v_add_f32_e32 v202, v202, v60
	v_exp_f32_e32 v62, v62
	v_add_f32_e32 v83, v83, v61
	v_exp_f32_e32 v63, v63
	v_add_f32_e32 v200, v200, v62
	v_exp_f32_e32 v64, v64
	v_add_f32_e32 v201, v201, v63
	v_exp_f32_e32 v65, v65
	v_add_f32_e32 v202, v202, v64
	v_add_f32_e32 v83, v83, v65
	v_add_f32_e32 v200, v200, v201
	v_add_f32_e32 v202, v202, v83
	v_add_f32_e32 v200, v200, v202
	v_add_f32_e32 v82, v82, v200
	v_max3_f32 v84, v2, v3, v4
	v_max3_f32 v85, v18, v19, v20
	v_max3_f32 v84, v84, v5, v6
	v_max3_f32 v85, v85, v21, v22
	v_max3_f32 v84, v84, v7, v8
	v_max3_f32 v85, v85, v23, v24
	v_max3_f32 v84, v84, v9, v10
	v_max3_f32 v85, v85, v25, v26
	v_max3_f32 v84, v84, v11, v12
	v_max3_f32 v85, v85, v27, v28
	v_max3_f32 v84, v84, v13, v14
	v_max3_f32 v85, v85, v29, v30
	v_max3_f32 v84, v84, v15, v16
	v_max3_f32 v85, v85, v31, v32
	v_max3_f32 v84, v84, v17, v33
	s_nop 0
	v_max_f32_e32 v84, v84, v85
	s_nop 0
	v_cmp_lt_f32_e32 vcc, s11, v84
	s_cbranch_vccnz .Lp1_rare_d1t0
.Lp1_back_d1t0:
	v_mov_b32_e32 v200, 0
	v_mov_b32_e32 v201, 0
	v_mov_b32_e32 v202, 0
	v_mov_b32_e32 v83, 0
	v_exp_f32_e32 v2, v2
	v_exp_f32_e32 v3, v3
	v_add_f32_e32 v200, v200, v2
	v_exp_f32_e32 v4, v4
	v_add_f32_e32 v201, v201, v3
	v_exp_f32_e32 v5, v5
	s_waitcnt lgkmcnt(7)
	v_mfma_f32_32x32x16_f16 v[34:49], v[204:207], v[108:111], v[130:145]
	v_add_f32_e32 v202, v202, v4
	v_exp_f32_e32 v6, v6
	v_add_f32_e32 v83, v83, v5
	v_exp_f32_e32 v7, v7
	v_add_f32_e32 v200, v200, v6
	v_exp_f32_e32 v8, v8
	s_waitcnt lgkmcnt(6)
	v_mfma_f32_32x32x16_f16 v[50:65], v[208:211], v[108:111], v[130:145]
	v_add_f32_e32 v201, v201, v7
	v_exp_f32_e32 v9, v9
	v_add_f32_e32 v202, v202, v8
	v_exp_f32_e32 v10, v10
	v_add_f32_e32 v83, v83, v9
	v_exp_f32_e32 v11, v11
	s_waitcnt lgkmcnt(5)
	v_mfma_f32_32x32x16_f16 v[34:49], v[212:215], v[104:107], v[34:49]
	v_add_f32_e32 v200, v200, v10
	v_exp_f32_e32 v12, v12
	v_add_f32_e32 v201, v201, v11
	v_exp_f32_e32 v13, v13
	v_add_f32_e32 v202, v202, v12
	v_exp_f32_e32 v14, v14
	s_waitcnt lgkmcnt(4)
	v_mfma_f32_32x32x16_f16 v[50:65], v[216:219], v[104:107], v[50:65]
	v_add_f32_e32 v83, v83, v13
	v_exp_f32_e32 v15, v15
	v_add_f32_e32 v200, v200, v14
	v_exp_f32_e32 v16, v16
	v_add_f32_e32 v201, v201, v15
	v_exp_f32_e32 v17, v17
	s_waitcnt lgkmcnt(3)
	v_mfma_f32_32x32x16_f16 v[34:49], v[220:223], v[100:103], v[34:49]
	v_add_f32_e32 v202, v202, v16
	v_exp_f32_e32 v18, v18
	v_add_f32_e32 v83, v83, v17
	v_exp_f32_e32 v19, v19
	v_add_f32_e32 v200, v200, v18
	v_exp_f32_e32 v20, v20
	s_waitcnt lgkmcnt(2)
	v_mfma_f32_32x32x16_f16 v[50:65], v[224:227], v[100:103], v[50:65]
	v_add_f32_e32 v201, v201, v19
	v_exp_f32_e32 v21, v21
	v_add_f32_e32 v202, v202, v20
	v_exp_f32_e32 v22, v22
	v_add_f32_e32 v83, v83, v21
	v_exp_f32_e32 v23, v23
	s_waitcnt lgkmcnt(1)
	v_mfma_f32_32x32x16_f16 v[34:49], v[228:231], v[96:99], v[34:49]
	v_add_f32_e32 v200, v200, v22
	v_exp_f32_e32 v24, v24
	v_add_f32_e32 v201, v201, v23
	v_exp_f32_e32 v25, v25
	v_add_f32_e32 v202, v202, v24
	v_exp_f32_e32 v26, v26
	s_waitcnt lgkmcnt(0)
	v_mfma_f32_32x32x16_f16 v[50:65], v[232:235], v[96:99], v[50:65]
	ds_read_b128 v[168:171], v167 offset:18432
	ds_read_b128 v[172:175], v167 offset:23040
	ds_read_b128 v[176:179], v167 offset:18464
	ds_read_b128 v[180:183], v167 offset:23072
	ds_read_b128 v[184:187], v167 offset:18496
	ds_read_b128 v[188:191], v167 offset:23104
	ds_read_b128 v[192:195], v167 offset:18528
	ds_read_b128 v[196:199], v167 offset:23136
	v_add_f32_e32 v83, v83, v25
	v_exp_f32_e32 v27, v27
	v_add_f32_e32 v200, v200, v26
	v_exp_f32_e32 v28, v28
	v_add_f32_e32 v201, v201, v27
	v_exp_f32_e32 v29, v29
	v_add_f32_e32 v202, v202, v28
	v_exp_f32_e32 v30, v30
	v_add_f32_e32 v83, v83, v29
	v_exp_f32_e32 v31, v31
	v_add_f32_e32 v200, v200, v30
	v_exp_f32_e32 v32, v32
	v_add_f32_e32 v201, v201, v31
	v_exp_f32_e32 v33, v33
	v_add_f32_e32 v202, v202, v32
	v_add_f32_e32 v83, v83, v33
	v_add_f32_e32 v200, v200, v201
	v_add_f32_e32 v202, v202, v83
	v_add_f32_e32 v200, v200, v202
	v_add_f32_e32 v82, v82, v200
	v_max3_f32 v84, v34, v35, v36
	v_max3_f32 v85, v50, v51, v52
	v_max3_f32 v84, v84, v37, v38
	v_max3_f32 v85, v85, v53, v54
	v_max3_f32 v84, v84, v39, v40
	v_max3_f32 v85, v85, v55, v56
	v_max3_f32 v84, v84, v41, v42
	v_max3_f32 v85, v85, v57, v58
	v_max3_f32 v84, v84, v43, v44
	v_max3_f32 v85, v85, v59, v60
	v_max3_f32 v84, v84, v45, v46
	v_max3_f32 v85, v85, v61, v62
	v_max3_f32 v84, v84, v47, v48
	v_max3_f32 v85, v85, v63, v64
	v_max3_f32 v84, v84, v49, v65
	s_nop 0
	v_max_f32_e32 v84, v84, v85
	s_nop 0
	v_cmp_lt_f32_e32 vcc, s11, v84
	s_cbranch_vccnz .Lp1_rare_d1t1
.Lp1_back_d1t1:
	v_mov_b32_e32 v200, 0
	v_mov_b32_e32 v201, 0
	v_mov_b32_e32 v202, 0
	v_mov_b32_e32 v83, 0
	v_exp_f32_e32 v34, v34
	v_exp_f32_e32 v35, v35
	v_add_f32_e32 v200, v200, v34
	v_exp_f32_e32 v36, v36
	v_add_f32_e32 v201, v201, v35
	v_exp_f32_e32 v37, v37
	s_waitcnt lgkmcnt(7)
	v_mfma_f32_32x32x16_f16 v[2:17], v[168:171], v[108:111], v[130:145]
	v_add_f32_e32 v202, v202, v36
	v_exp_f32_e32 v38, v38
	v_add_f32_e32 v83, v83, v37
	v_exp_f32_e32 v39, v39
	v_add_f32_e32 v200, v200, v38
	v_exp_f32_e32 v40, v40
	s_waitcnt lgkmcnt(6)
	v_mfma_f32_32x32x16_f16 v[18:33], v[172:175], v[108:111], v[130:145]
	v_add_f32_e32 v201, v201, v39
	v_exp_f32_e32 v41, v41
	v_add_f32_e32 v202, v202, v40
	v_exp_f32_e32 v42, v42
	v_add_f32_e32 v83, v83, v41
	v_exp_f32_e32 v43, v43
	s_waitcnt lgkmcnt(5)
	v_mfma_f32_32x32x16_f16 v[2:17], v[176:179], v[104:107], v[2:17]
	v_add_f32_e32 v200, v200, v42
	v_exp_f32_e32 v44, v44
	v_add_f32_e32 v201, v201, v43
	v_exp_f32_e32 v45, v45
	v_add_f32_e32 v202, v202, v44
	v_exp_f32_e32 v46, v46
	s_waitcnt lgkmcnt(4)
	v_mfma_f32_32x32x16_f16 v[18:33], v[180:183], v[104:107], v[18:33]
	v_add_f32_e32 v83, v83, v45
	v_exp_f32_e32 v47, v47
	v_add_f32_e32 v200, v200, v46
	v_exp_f32_e32 v48, v48
	v_add_f32_e32 v201, v201, v47
	v_exp_f32_e32 v49, v49
	s_waitcnt lgkmcnt(3)
	v_mfma_f32_32x32x16_f16 v[2:17], v[184:187], v[100:103], v[2:17]
	v_add_f32_e32 v202, v202, v48
	v_exp_f32_e32 v50, v50
	v_add_f32_e32 v83, v83, v49
	v_exp_f32_e32 v51, v51
	v_add_f32_e32 v200, v200, v50
	v_exp_f32_e32 v52, v52
	s_waitcnt lgkmcnt(2)
	v_mfma_f32_32x32x16_f16 v[18:33], v[188:191], v[100:103], v[18:33]
	v_add_f32_e32 v201, v201, v51
	v_exp_f32_e32 v53, v53
	v_add_f32_e32 v202, v202, v52
	v_exp_f32_e32 v54, v54
	v_add_f32_e32 v83, v83, v53
	v_exp_f32_e32 v55, v55
	s_waitcnt lgkmcnt(1)
	v_mfma_f32_32x32x16_f16 v[2:17], v[192:195], v[96:99], v[2:17]
	v_add_f32_e32 v200, v200, v54
	v_exp_f32_e32 v56, v56
	v_add_f32_e32 v201, v201, v55
	v_exp_f32_e32 v57, v57
	v_add_f32_e32 v202, v202, v56
	v_exp_f32_e32 v58, v58
	s_waitcnt lgkmcnt(0)
	v_mfma_f32_32x32x16_f16 v[18:33], v[196:199], v[96:99], v[18:33]
	ds_read_b128 v[204:207], v167 offset:27648
	ds_read_b128 v[208:211], v167 offset:32256
	ds_read_b128 v[212:215], v167 offset:27680
	ds_read_b128 v[216:219], v167 offset:32288
	ds_read_b128 v[220:223], v167 offset:27712
	ds_read_b128 v[224:227], v167 offset:32320
	ds_read_b128 v[228:231], v167 offset:27744
	ds_read_b128 v[232:235], v167 offset:32352
	v_add_f32_e32 v83, v83, v57
	v_exp_f32_e32 v59, v59
	v_add_f32_e32 v200, v200, v58
	v_exp_f32_e32 v60, v60
	v_add_f32_e32 v201, v201, v59
	v_exp_f32_e32 v61, v61
	v_add_f32_e32 v202, v202, v60
	v_exp_f32_e32 v62, v62
	v_add_f32_e32 v83, v83, v61
	v_exp_f32_e32 v63, v63
	v_add_f32_e32 v200, v200, v62
	v_exp_f32_e32 v64, v64
	v_add_f32_e32 v201, v201, v63
	v_exp_f32_e32 v65, v65
	v_add_f32_e32 v202, v202, v64
	v_add_f32_e32 v83, v83, v65
	v_add_f32_e32 v200, v200, v201
	v_add_f32_e32 v202, v202, v83
	v_add_f32_e32 v200, v200, v202
	v_add_f32_e32 v82, v82, v200
	v_max3_f32 v84, v2, v3, v4
	v_max3_f32 v85, v18, v19, v20
	v_max3_f32 v84, v84, v5, v6
	v_max3_f32 v85, v85, v21, v22
	v_max3_f32 v84, v84, v7, v8
	v_max3_f32 v85, v85, v23, v24
	v_max3_f32 v84, v84, v9, v10
	v_max3_f32 v85, v85, v25, v26
	v_max3_f32 v84, v84, v11, v12
	v_max3_f32 v85, v85, v27, v28
	v_max3_f32 v84, v84, v13, v14
	v_max3_f32 v85, v85, v29, v30
	v_max3_f32 v84, v84, v15, v16
	v_max3_f32 v85, v85, v31, v32
	v_max3_f32 v84, v84, v17, v33
	s_nop 0
	v_max_f32_e32 v84, v84, v85
	s_nop 0
	v_cmp_lt_f32_e32 vcc, s11, v84
	s_cbranch_vccnz .Lp1_rare_d1t2

.Lp1_back_d1t3:
	s_add_i32 s15, s15, 8
	s_cmp_lt_u32 s15, 32
	s_waitcnt lgkmcnt(0)
	s_barrier
	s_cbranch_scc1 .Lp1_loop
	s_branch .Lp1_fin

.Lp1_fin:
	s_lshl_b64 s[0:1], s[20:21], 1
	s_add_u32 s0, s18, s0
	s_addc_u32 s1, s19, s1
	global_load_dwordx4 v[2:5], v[66:67], off
	global_load_dwordx4 v[6:9], v[68:69], off
	v_lshlrev_b32_e32 v10, 1, v79
	global_load_dwordx4 v[10:13], v10, s[0:1]
	v_lshlrev_b32_e32 v14, 1, v80
	global_load_dwordx4 v[14:17], v14, s[0:1]
	v_mov_b32_e32 v200, 0
	v_mov_b32_e32 v201, 0
	v_mov_b32_e32 v202, 0
	v_mov_b32_e32 v83, 0
	v_exp_f32_e32 v34, v34
	v_exp_f32_e32 v35, v35
	v_add_f32_e32 v200, v200, v34
	v_exp_f32_e32 v36, v36
	v_add_f32_e32 v201, v201, v35
	v_exp_f32_e32 v37, v37
	v_add_f32_e32 v202, v202, v36
	v_exp_f32_e32 v38, v38
	v_add_f32_e32 v83, v83, v37
	v_exp_f32_e32 v39, v39
	v_add_f32_e32 v200, v200, v38
	v_exp_f32_e32 v40, v40
	v_add_f32_e32 v201, v201, v39
	v_exp_f32_e32 v41, v41
	v_add_f32_e32 v202, v202, v40
	v_exp_f32_e32 v42, v42
	v_add_f32_e32 v83, v83, v41
	v_exp_f32_e32 v43, v43
	v_add_f32_e32 v200, v200, v42
	v_exp_f32_e32 v44, v44
	v_add_f32_e32 v201, v201, v43
	v_exp_f32_e32 v45, v45
	v_add_f32_e32 v202, v202, v44
	v_exp_f32_e32 v46, v46
	v_add_f32_e32 v83, v83, v45
	v_exp_f32_e32 v47, v47
	v_add_f32_e32 v200, v200, v46
	v_exp_f32_e32 v48, v48
	v_add_f32_e32 v201, v201, v47
	v_exp_f32_e32 v49, v49
	v_add_f32_e32 v202, v202, v48
	v_exp_f32_e32 v50, v50
	v_add_f32_e32 v83, v83, v49
	v_exp_f32_e32 v51, v51
	v_add_f32_e32 v200, v200, v50
	v_exp_f32_e32 v52, v52
	v_add_f32_e32 v201, v201, v51
	v_exp_f32_e32 v53, v53
	v_add_f32_e32 v202, v202, v52
	v_exp_f32_e32 v54, v54
	v_add_f32_e32 v83, v83, v53
	v_exp_f32_e32 v55, v55
	v_add_f32_e32 v200, v200, v54
	v_exp_f32_e32 v56, v56
	v_add_f32_e32 v201, v201, v55
	v_exp_f32_e32 v57, v57
	v_add_f32_e32 v202, v202, v56
	v_exp_f32_e32 v58, v58
	v_add_f32_e32 v83, v83, v57
	v_exp_f32_e32 v59, v59
	v_add_f32_e32 v200, v200, v58
	v_exp_f32_e32 v60, v60
	v_add_f32_e32 v201, v201, v59
	v_exp_f32_e32 v61, v61
	v_add_f32_e32 v202, v202, v60
	v_exp_f32_e32 v62, v62
	v_add_f32_e32 v83, v83, v61
	v_exp_f32_e32 v63, v63
	v_add_f32_e32 v200, v200, v62
	v_exp_f32_e32 v64, v64
	v_add_f32_e32 v201, v201, v63
	v_exp_f32_e32 v65, v65
	v_add_f32_e32 v202, v202, v64
	v_add_f32_e32 v83, v83, v65
	v_add_f32_e32 v200, v200, v201
	v_add_f32_e32 v202, v202, v83
	v_add_f32_e32 v200, v200, v202
	v_add_f32_e32 v82, v82, v200
	v_add_u32_e32 v167, 0x6000, v87
	v_add_u32_e32 v77, 0x6000, v88
	v_add_u32_e32 v78, 0x6000, v89
	s_barrier
	v_mbcnt_lo_u32_b32 v21, -1, 0
	v_mbcnt_hi_u32_b32 v21, -1, v21
	v_and_b32_e32 v23, 64, v21
	v_xor_b32_e32 v22, 32, v21
	v_add_u32_e32 v24, 64, v23
	v_cmp_lt_i32_e32 vcc, v22, v24
	v_cndmask_b32_e32 v21, v21, v22, vcc
	v_lshlrev_b32_e32 v21, 2, v21
	ds_bpermute_b32 v22, v21, v81
	v_mov_b32_e32 v18, v82
	ds_bpermute_b32 v19, v21, v18
	v_max_f32_e32 v21, v81, v81
	s_mov_b32 s15, 0
	s_waitcnt lgkmcnt(1)
	v_max_f32_e32 v20, v22, v22
	v_max_f32_e32 v20, v21, v20
	v_sub_f32_e32 v22, v22, v20
	v_sub_f32_e32 v21, v81, v20
	v_exp_f32_e32 v22, v22
	v_exp_f32_e32 v21, v21
	s_lshl_b64 s[18:19], s[14:15], 18
	v_mov_b32_e32 v131, 0
	s_waitcnt lgkmcnt(0)
	v_mul_f32_e32 v19, v22, v19
	v_fmac_f32_e32 v19, v18, v21
	v_div_scale_f32 v18, s[10:11], v19, v19, 1.0
	s_movk_i32 s10, 0x60
	s_nop 0
	v_mad_u32_u24 v188, v73, s10, v74
	v_mad_u32_u24 v189, v75, s10, v74
	s_waitcnt vmcnt(3)
	ds_write_b128 v77, v[2:5]
	s_waitcnt vmcnt(2)
	ds_write_b128 v78, v[6:9]
	v_lshlrev_b32_e32 v2, 1, v188
	s_waitcnt vmcnt(1)
	ds_write_b128 v2, v[10:13]
	v_lshlrev_b32_e32 v2, 1, v189
	s_mul_i32 s10, s14, 0x1200
	s_waitcnt vmcnt(0)
	ds_write_b128 v2, v[14:17]
	s_add_i32 s10, s10, 0xa800
	v_lshrrev_b32_e32 v2, 2, v0
	v_and_or_b32 v3, v2, 3, v1
	s_movk_i32 s11, 0x48
	v_mov_b32_e32 v5, s10
	v_add_u32_e32 v4, s10, v76
	v_mad_u32_u24 v5, v3, s11, v5
	s_lshl_b64 s[10:11], s[12:13], 24
	s_and_b32 s13, s2, 15
	s_lshl_b32 s13, s13, 20
	v_and_b32_e32 v0, 3, v0
	s_or_b32 s10, s10, s13
	v_and_or_b32 v0, v2, 4, v0
	s_add_u32 s10, s10, s18
	v_lshlrev_b32_e32 v0, 3, v0
	v_mul_u32_u24_e32 v2, 0xc0, v3
	v_lshlrev_b32_e32 v3, 13, v72
	s_addc_u32 s11, s11, s19
	v_or_b32_e32 v185, v2, v0
	v_or_b32_e32 v2, v3, v164
	s_add_u32 s10, s4, s10
	v_lshlrev_b32_e32 v130, 2, v2
	s_addc_u32 s11, s5, s11
	v_lshl_add_u64 v[2:3], s[10:11], 0, v[130:131]
	s_mov_b64 s[18:19], 0x80
	v_lshl_add_u64 v[132:133], v[2:3], 0, s[18:19]
	v_or_b32_e32 v2, 0x36000, v130
	v_mov_b32_e32 v3, v131
	v_lshl_add_u64 v[134:135], s[10:11], 0, v[2:3]
	v_or_b32_e32 v2, 0x2000, v130
	v_lshl_add_u64 v[2:3], s[10:11], 0, v[2:3]
	v_lshl_add_u64 v[136:137], v[2:3], 0, s[18:19]
	v_or_b32_e32 v2, 0x34000, v130
	v_mov_b32_e32 v3, v131
	v_rcp_f32_e32 v21, v18
	v_lshl_add_u64 v[138:139], s[10:11], 0, v[2:3]
	v_or_b32_e32 v2, 0x4000, v130
	v_lshl_add_u64 v[2:3], s[10:11], 0, v[2:3]
	v_lshl_add_u64 v[140:141], v[2:3], 0, s[18:19]
	v_or_b32_e32 v2, 0x32000, v130
	v_mov_b32_e32 v3, v131
	v_lshl_add_u64 v[142:143], s[10:11], 0, v[2:3]
	v_or_b32_e32 v2, 0x6000, v130
	v_fma_f32 v22, -v18, v21, 1.0
	v_lshl_add_u64 v[2:3], s[10:11], 0, v[2:3]
	v_fmac_f32_e32 v21, v22, v21
	v_div_scale_f32 v22, vcc, 1.0, v19, 1.0
	v_lshl_add_u64 v[144:145], v[2:3], 0, s[18:19]
	v_or_b32_e32 v2, 0x30000, v130
	v_mov_b32_e32 v3, v131
	v_mul_f32_e32 v24, v22, v21
	v_lshl_add_u64 v[146:147], s[10:11], 0, v[2:3]
	v_or_b32_e32 v2, 0x10000, v130
	v_fma_f32 v25, -v18, v24, v22
	v_lshl_add_u64 v[2:3], s[10:11], 0, v[2:3]
	v_fmac_f32_e32 v24, v25, v21
	v_lshl_add_u64 v[148:149], v[2:3], 0, s[18:19]
	v_or_b32_e32 v2, 0x26000, v130
	v_mov_b32_e32 v3, v131
	v_fma_f32 v18, -v18, v24, v22
	v_lshl_add_u64 v[150:151], s[10:11], 0, v[2:3]
	v_or_b32_e32 v2, 0x12000, v130
	v_div_fmas_f32 v18, v18, v21, v24
	v_lshlrev_b32_e32 v184, 2, v72
	v_lshl_add_u64 v[2:3], s[10:11], 0, v[2:3]
	v_div_fixup_f32 v18, v18, v19, 1.0
	v_or_b32_e32 v19, v184, v23
	v_lshl_add_u64 v[152:153], v[2:3], 0, s[18:19]
	v_or_b32_e32 v2, 0x24000, v130
	v_mov_b32_e32 v3, v131
	v_lshlrev_b32_e32 v19, 2, v19
	v_lshl_add_u64 v[154:155], s[10:11], 0, v[2:3]
	v_or_b32_e32 v2, 0x14000, v130
	ds_bpermute_b32 v33, v19, v20 offset:36
	ds_bpermute_b32 v32, v19, v20 offset:40
	ds_bpermute_b32 v35, v19, v20 offset:44
	ds_bpermute_b32 v34, v19, v20 offset:64
	ds_bpermute_b32 v37, v19, v20 offset:68
	ds_bpermute_b32 v36, v19, v20 offset:72
	ds_bpermute_b32 v39, v19, v20 offset:76
	ds_bpermute_b32 v38, v19, v20 offset:96
	ds_bpermute_b32 v41, v19, v20 offset:100
	ds_bpermute_b32 v40, v19, v20 offset:104
	ds_bpermute_b32 v43, v19, v20 offset:108
	v_lshl_add_u64 v[2:3], s[10:11], 0, v[2:3]
	ds_bpermute_b32 v46, v19, v20 offset:32
	ds_bpermute_b32 v47, v19, v20 offset:12
	ds_bpermute_b32 v42, v19, v20 offset:8
	ds_bpermute_b32 v45, v19, v20 offset:4
	ds_bpermute_b32 v44, v19, v20
	ds_bpermute_b32 v183, v19, v18
	ds_bpermute_b32 v182, v19, v18 offset:4
	ds_bpermute_b32 v181, v19, v18 offset:8
	ds_bpermute_b32 v180, v19, v18 offset:12
	ds_bpermute_b32 v179, v19, v18 offset:32
	ds_bpermute_b32 v178, v19, v18 offset:36
	ds_bpermute_b32 v177, v19, v18 offset:40
	ds_bpermute_b32 v176, v19, v18 offset:44
	ds_bpermute_b32 v175, v19, v18 offset:64
	ds_bpermute_b32 v174, v19, v18 offset:68
	ds_bpermute_b32 v173, v19, v18 offset:72
	ds_bpermute_b32 v172, v19, v18 offset:76
	ds_bpermute_b32 v171, v19, v18 offset:96
	ds_bpermute_b32 v170, v19, v18 offset:100
	ds_bpermute_b32 v169, v19, v18 offset:104
	ds_bpermute_b32 v168, v19, v18 offset:108
	v_lshl_add_u64 v[156:157], v[2:3], 0, s[18:19]
	v_or_b32_e32 v2, 0x22000, v130
	v_mov_b32_e32 v3, v131
	v_lshl_add_u64 v[158:159], s[10:11], 0, v[2:3]
	v_or_b32_e32 v2, 0x16000, v130
	v_lshl_add_u64 v[2:3], s[10:11], 0, v[2:3]
	v_lshl_add_u64 v[160:161], v[2:3], 0, s[18:19]
	v_or_b32_e32 v2, 0x20000, v130
	v_mov_b32_e32 v3, v131
	v_add_u32_e32 v187, v4, v1
	v_lshl_add_u64 v[162:163], s[10:11], 0, v[2:3]
	s_mov_b64 s[10:11], 0
	s_movk_i32 s13, 0x3000
	s_waitcnt lgkmcnt(14)
	v_xor_b32_e32 v63, 0x80000000, v43
	v_xor_b32_e32 v62, 0x80000000, v40
	v_xor_b32_e32 v61, 0x80000000, v41
	v_xor_b32_e32 v60, 0x80000000, v38
	v_xor_b32_e32 v59, 0x80000000, v39
	v_xor_b32_e32 v58, 0x80000000, v36
	v_xor_b32_e32 v57, 0x80000000, v37
	v_xor_b32_e32 v56, 0x80000000, v34
	v_xor_b32_e32 v55, 0x80000000, v35
	v_xor_b32_e32 v54, 0x80000000, v32
	v_xor_b32_e32 v53, 0x80000000, v33
	v_add_u32_e32 v186, v5, v0
	v_xor_b32_e32 v52, 0x80000000, v46
	v_xor_b32_e32 v51, 0x80000000, v47
	v_xor_b32_e32 v50, 0x80000000, v42
	v_xor_b32_e32 v49, 0x80000000, v45
	v_xor_b32_e32 v48, 0x80000000, v44
	v_mov_b32_e32 v0, v131
	v_mov_b32_e32 v1, v131
	v_mov_b32_e32 v2, v131
	v_mov_b32_e32 v4, v131
	v_mov_b32_e32 v5, v131
	v_mov_b32_e32 v6, v131
	v_mov_b32_e32 v7, v131
	v_mov_b32_e32 v8, v131
	v_mov_b32_e32 v9, v131
	v_mov_b32_e32 v10, v131
	v_mov_b32_e32 v11, v131
	v_mov_b32_e32 v12, v131
	v_mov_b32_e32 v13, v131
	v_mov_b32_e32 v14, v131
	v_mov_b32_e32 v15, v131
	v_mov_b32_e32 v16, v131
	v_mov_b32_e32 v17, v131
	v_mov_b32_e32 v18, v131
	v_mov_b32_e32 v19, v131
	v_mov_b32_e32 v20, v131
	v_mov_b32_e32 v21, v131
	v_mov_b32_e32 v22, v131
	v_mov_b32_e32 v23, v131
	v_mov_b32_e32 v24, v131
	v_mov_b32_e32 v25, v131
	v_mov_b32_e32 v26, v131
	v_mov_b32_e32 v27, v131
	v_mov_b32_e32 v28, v131
	v_mov_b32_e32 v29, v131
	v_mov_b32_e32 v30, v131
	v_mov_b32_e32 v31, v131
	v_add_u32_e32 v131, 0x800, v187
	s_waitcnt lgkmcnt(0)
	s_barrier

	.amdhsa_kernel _Z11attn_kernelILi0EEvPKDF16_S1_S1_PKfS3_PfPDF16_
		.amdhsa_group_segment_fixed_size 73728
		.amdhsa_private_segment_fixed_size 0
		.amdhsa_kernarg_size 56
		.amdhsa_user_sgpr_count 2
		.amdhsa_user_sgpr_dispatch_ptr 0
		.amdhsa_user_sgpr_queue_ptr 0
		.amdhsa_user_sgpr_kernarg_segment_ptr 1
		.amdhsa_user_sgpr_dispatch_id 0
		.amdhsa_user_sgpr_kernarg_preload_length 0
		.amdhsa_user_sgpr_kernarg_preload_offset 0
		.amdhsa_user_sgpr_private_segment_size 0
		.amdhsa_uses_dynamic_stack 0
		.amdhsa_enable_private_segment 0
		.amdhsa_system_sgpr_workgroup_id_x 1
		.amdhsa_system_sgpr_workgroup_id_y 0
		.amdhsa_system_sgpr_workgroup_id_z 0
		.amdhsa_system_sgpr_workgroup_info 0
		.amdhsa_system_vgpr_workitem_id 0
		.amdhsa_next_free_vgpr 236
		.amdhsa_next_free_sgpr 96
		.amdhsa_accum_offset 236
		.amdhsa_reserve_vcc 1
		.amdhsa_float_round_mode_32 0
		.amdhsa_float_round_mode_16_64 0
		.amdhsa_float_denorm_mode_32 3
		.amdhsa_float_denorm_mode_16_64 3
		.amdhsa_dx10_clamp 1
		.amdhsa_ieee_mode 1
		.amdhsa_fp16_overflow 0
		.amdhsa_tg_split 0
		.amdhsa_exception_fp_ieee_invalid_op 0
		.amdhsa_exception_fp_denorm_src 0
		.amdhsa_exception_fp_ieee_div_zero 0
		.amdhsa_exception_fp_ieee_overflow 0
		.amdhsa_exception_fp_ieee_underflow 0
		.amdhsa_exception_fp_ieee_inexact 0
		.amdhsa_exception_int_div_zero 0
	.end_amdhsa_kernel

amdhsa.kernels:
  - .agpr_count:     0
    .args:
      - .actual_access:  read_only
        .address_space:  global
        .offset:         0
        .size:           8
        .value_kind:     global_buffer
      - .actual_access:  read_only
        .address_space:  global
        .offset:         8
        .size:           8
        .value_kind:     global_buffer
      - .actual_access:  read_only
        .address_space:  global
        .offset:         16
        .size:           8
        .value_kind:     global_buffer
      - .actual_access:  read_only
        .address_space:  global
        .offset:         24
        .size:           8
        .value_kind:     global_buffer
      - .actual_access:  read_only
        .address_space:  global
        .offset:         32
        .size:           8
        .value_kind:     global_buffer
      - .actual_access:  write_only
        .address_space:  global
        .offset:         40
        .size:           8
        .value_kind:     global_buffer
      - .actual_access:  write_only
        .address_space:  global
        .offset:         48
        .size:           8
        .value_kind:     global_buffer
    .group_segment_fixed_size: 0
    .kernarg_segment_align: 8
    .kernarg_segment_size: 56
    .language:       OpenCL C
    .language_version:
      - 2
      - 0
    .max_flat_workgroup_size: 256
    .name:           _Z10cvt_kernelPKfS0_S0_S0_S0_PDF16_S1_
    .private_segment_fixed_size: 0
    .sgpr_count:     22
    .sgpr_spill_count: 0
    .symbol:         _Z10cvt_kernelPKfS0_S0_S0_S0_PDF16_S1_.kd
    .uniform_work_group_size: 1
    .uses_dynamic_stack: false
    .vgpr_count:     14
    .vgpr_spill_count: 0
    .wavefront_size: 64
  - .agpr_count:     0
    .args:
      - .actual_access:  read_only
        .address_space:  global
        .offset:         0
        .size:           8
        .value_kind:     global_buffer
      - .actual_access:  read_only
        .address_space:  global
        .offset:         8
        .size:           8
        .value_kind:     global_buffer
      - .actual_access:  write_only
        .address_space:  global
        .offset:         16
        .size:           8
        .value_kind:     global_buffer
      - .actual_access:  write_only
        .address_space:  global
        .offset:         24
        .size:           8
        .value_kind:     global_buffer
    .group_segment_fixed_size: 18432
    .kernarg_segment_align: 8
    .kernarg_segment_size: 32
    .language:       OpenCL C
    .language_version:
      - 2
      - 0
    .max_flat_workgroup_size: 256
    .name:           _Z12stats_kernelPKDF16_S0_PfS1_
    .private_segment_fixed_size: 0
    .sgpr_count:     19
    .sgpr_spill_count: 0
    .symbol:         _Z12stats_kernelPKDF16_S0_PfS1_.kd
    .uniform_work_group_size: 1
    .uses_dynamic_stack: false
    .vgpr_count:     100
    .vgpr_spill_count: 0
    .wavefront_size: 64
  - .agpr_count:     0
    .args:
      - .actual_access:  read_only
        .address_space:  global
        .offset:         0
        .size:           8
        .value_kind:     global_buffer
      - .actual_access:  read_only
        .address_space:  global
        .offset:         8
        .size:           8
        .value_kind:     global_buffer
      - .actual_access:  read_only
        .address_space:  global
        .offset:         16
        .size:           8
        .value_kind:     global_buffer
      - .actual_access:  read_only
        .address_space:  global
        .offset:         24
        .size:           8
        .value_kind:     global_buffer
      - .actual_access:  write_only
        .address_space:  global
        .offset:         32
        .size:           8
        .value_kind:     global_buffer
      - .actual_access:  write_only
        .address_space:  global
        .offset:         40
        .size:           8
        .value_kind:     global_buffer
      - .actual_access:  write_only
        .address_space:  global
        .offset:         48
        .size:           8
        .value_kind:     global_buffer
      - .actual_access:  read_only
        .address_space:  global
        .offset:         56
        .size:           8
        .value_kind:     global_buffer
      - .offset:         64
        .size:           4
        .value_kind:     by_value
    .group_segment_fixed_size: 0
    .kernarg_segment_align: 8
    .kernarg_segment_size: 68
    .language:       OpenCL C
    .language_version:
      - 2
      - 0
    .max_flat_workgroup_size: 512
    .name:           _Z11gemm_kernelILi256ELi192ELi4ELi2ELi0EEvPKDF16_S1_PKfS3_PDF16_S4_S4_Pfi
    .private_segment_fixed_size: 0
    .sgpr_count:     27
    .sgpr_spill_count: 0
    .symbol:         _Z11gemm_kernelILi256ELi192ELi4ELi2ELi0EEvPKDF16_S1_PKfS3_PDF16_S4_S4_Pfi.kd
    .uniform_work_group_size: 1
    .uses_dynamic_stack: false
    .vgpr_count:     249
    .vgpr_spill_count: 0
    .wavefront_size: 64
  - .agpr_count:     0
    .args:
      - .actual_access:  read_only
        .address_space:  global
        .offset:         0
        .size:           8
        .value_kind:     global_buffer
      - .actual_access:  read_only
        .address_space:  global
        .offset:         8
        .size:           8
        .value_kind:     global_buffer
      - .actual_access:  read_only
        .address_space:  global
        .offset:         16
        .size:           8
        .value_kind:     global_buffer
      - .actual_access:  read_only
        .address_space:  global
        .offset:         24
        .size:           8
        .value_kind:     global_buffer
      - .actual_access:  read_only
        .address_space:  global
        .offset:         32
        .size:           8
        .value_kind:     global_buffer
      - .actual_access:  read_only
        .address_space:  global
        .offset:         40
        .size:           8
        .value_kind:     global_buffer
      - .actual_access:  read_only
        .address_space:  global
        .offset:         48
        .size:           8
        .value_kind:     global_buffer
      - .actual_access:  write_only
        .address_space:  global
        .offset:         56
        .size:           8
        .value_kind:     global_buffer
      - .offset:         64
        .size:           4
        .value_kind:     by_value
    .group_segment_fixed_size: 0
    .kernarg_segment_align: 8
    .kernarg_segment_size: 68
    .language:       OpenCL C
    .language_version:
      - 2
      - 0
    .max_flat_workgroup_size: 512
    .name:           _Z11gemm_kernelILi128ELi128ELi4ELi2ELi1EEvPKDF16_S1_PKfS3_PDF16_S4_S4_Pfi
    .private_segment_fixed_size: 0
    .sgpr_count:     19
    .sgpr_spill_count: 0
    .symbol:         _Z11gemm_kernelILi128ELi128ELi4ELi2ELi1EEvPKDF16_S1_PKfS3_PDF16_S4_S4_Pfi.kd
    .uniform_work_group_size: 1
    .uses_dynamic_stack: false
    .vgpr_count:     88
    .vgpr_spill_count: 0
    .wavefront_size: 64
  - .agpr_count:     0
    .args:
      - .actual_access:  read_only
        .address_space:  global
        .offset:         0
        .size:           8
        .value_kind:     global_buffer
      - .actual_access:  read_only
        .address_space:  global
        .offset:         8
        .size:           8
        .value_kind:     global_buffer
      - .actual_access:  read_only
        .address_space:  global
        .offset:         16
        .size:           8
        .value_kind:     global_buffer
      - .actual_access:  read_only
        .address_space:  global
        .offset:         24
        .size:           8
        .value_kind:     global_buffer
      - .actual_access:  read_only
        .address_space:  global
        .offset:         32
        .size:           8
        .value_kind:     global_buffer
      - .actual_access:  write_only
        .address_space:  global
        .offset:         40
        .size:           8
        .value_kind:     global_buffer
      - .actual_access:  write_only
        .address_space:  global
        .offset:         48
        .size:           8
        .value_kind:     global_buffer
    .group_segment_fixed_size: 73728
    .kernarg_segment_align: 8
    .kernarg_segment_size: 56
    .language:       OpenCL C
    .language_version:
      - 2
      - 0
    .max_flat_workgroup_size: 256
    .name:           _Z11attn_kernelILi0EEvPKDF16_S1_S1_PKfS3_PfPDF16_
    .private_segment_fixed_size: 0
    .sgpr_count:     30
    .sgpr_spill_count: 0
    .symbol:         _Z11attn_kernelILi0EEvPKDF16_S1_S1_PKfS3_PfPDF16_.kd
    .uniform_work_group_size: 1
    .uses_dynamic_stack: false
    .vgpr_count:     236
    .vgpr_spill_count: 0
    .wavefront_size: 64
